# v025
# speedup vs baseline: 1.1039x; 1.0114x over previous
.LBB2_24:
	s_add_i32 s51, s51, 1
	s_and_b64 vcc, exec, s[28:29]
	s_mov_b32 s91, s84
	s_mov_b32 s27, s85
	s_mov_b32 s34, s86
	s_mov_b32 s30, s26
	s_mov_b32 s94, s87
	s_mov_b32 s93, s88
	s_mov_b32 s92, s89
	s_mov_b32 s35, s90
	s_cbranch_vccnz .LBB2_93
	s_cmpk_gt_u32 s33, 0xff
	s_cbranch_scc0 .Lmy_restag_skip
	s_barrier
.Lmy_restag_skip:
.LBB2_25:
	s_cmp_lg_u32 s51, 0
	s_cselect_b64 s[0:1], -1, 0
	s_or_b64 s[28:29], s[0:1], s[10:11]
	s_and_b64 vcc, exec, s[28:29]
	s_cbranch_vccnz .LBB2_27
	s_mov_b32 s84, s79
	s_mov_b32 s85, s67
	s_mov_b32 s86, s69
	s_mov_b32 s26, s68
	s_mov_b32 s87, s83
	s_mov_b32 s88, s80
	s_mov_b32 s89, s82
	s_mov_b32 s90, s81

.LBB2_36:
	s_waitcnt vmcnt(6) lgkmcnt(0)
	s_cmpk_gt_u32 s33, 0xff
	s_cbranch_scc1 .Lmy_destag_skip
	s_barrier
.Lmy_destag_skip:
	s_mov_b32 s96, 0xc038aa3b
	s_mov_b32 s98, 0x3b800000
	s_nop 15
	s_nop 15
	v_lshl_or_b32 v210, s91, 6, v229
	v_lshl_add_u32 v208, s27, 8, v227
	s_cmp_lg_u32 s30, 0
	v_or_b32_e32 v206, 16, v208
	v_or_b32_e32 v204, 32, v208
	v_or_b32_e32 v202, 48, v208
	v_add_u32_e32 v200, 0x80, v208
	v_ashrrev_i32_e32 v211, 31, v210
	s_cbranch_scc1 .LBB2_38
	s_ashr_i32 s35, s34, 31
	v_mad_i64_i32 v[128:129], s[36:37], v208, 28, s[34:35]
	v_lshl_add_u64 v[218:219], v[210:211], 4, s[6:7]
	v_lshl_add_u64 v[128:129], v[128:129], 4, s[4:5]
	global_load_dwordx4 v[164:167], v[218:219], off offset:16
	global_load_dwordx4 v[172:175], v[218:219], off
	global_load_dwordx4 v[156:159], v[128:129], off
	global_load_dwordx4 v[168:171], v[218:219], off offset:32
	global_load_dwordx4 v[160:163], v[218:219], off offset:48
	v_mad_i64_i32 v[128:129], s[36:37], v206, 28, s[34:35]
	v_lshl_add_u64 v[128:129], v[128:129], 4, s[4:5]
	global_load_dwordx4 v[152:155], v[128:129], off
	v_mad_i64_i32 v[128:129], s[36:37], v204, 28, s[34:35]
	v_lshl_add_u64 v[128:129], v[128:129], 4, s[4:5]
	global_load_dwordx4 v[148:151], v[128:129], off
	v_mad_i64_i32 v[128:129], s[36:37], v202, 28, s[34:35]
	v_lshl_add_u64 v[128:129], v[128:129], 4, s[4:5]
	global_load_dwordx4 v[144:147], v[128:129], off
	v_add_u32_e32 v130, 0x90, v208
	v_add_u32_e32 v132, 0xa0, v208
	v_add_u32_e32 v134, 0xb0, v208
	v_mad_i64_i32 v[128:129], s[36:37], v200, 28, s[34:35]
	v_mad_i64_i32 v[130:131], s[36:37], v130, 28, s[34:35]
	v_mad_i64_i32 v[132:133], s[36:37], v132, 28, s[34:35]
	v_mad_i64_i32 v[134:135], s[36:37], v134, 28, s[34:35]
	v_lshl_add_u64 v[128:129], v[128:129], 4, s[4:5]
	v_lshl_add_u64 v[130:131], v[130:131], 4, s[4:5]
	v_lshl_add_u64 v[132:133], v[132:133], 4, s[4:5]
	v_lshl_add_u64 v[176:177], v[134:135], 4, s[4:5]
	global_load_dwordx4 v[140:143], v[128:129], off
	global_load_dwordx4 v[136:139], v[130:131], off
	s_nop 0
	global_load_dwordx4 v[132:135], v[132:133], off
	s_nop 0
	global_load_dwordx4 v[128:131], v[176:177], off
	s_movk_i32 s31, 0x4000
	s_waitcnt vmcnt(11)
	v_mov_b32_e32 v190, v164
	s_waitcnt vmcnt(10)
	v_mov_b32_e32 v191, v173
	v_mov_b32_e32 v173, v165
	v_mov_b32_e32 v164, v174
	v_mov_b32_e32 v165, v166
	v_mov_b32_e32 v166, v175
	s_waitcnt vmcnt(9)
	v_pk_mul_f32 v[174:175], v[156:157], v[190:191]
	s_waitcnt vmcnt(8)
	v_mul_f32_e32 v176, v157, v169
	s_waitcnt vmcnt(7)
	v_mul_f32_e32 v182, v156, v160
	v_pk_mul_f32 v[184:185], v[158:159], v[162:163]
	v_pk_fma_f32 v[174:175], v[156:157], v[172:173], v[174:175] op_sel:[0,0,1] op_sel_hi:[1,1,0]
	v_pk_fma_f32 v[176:177], v[156:157], v[168:169], v[176:177] op_sel_hi:[1,1,0]
	v_pk_fma_f32 v[182:183], v[156:157], v[160:161], v[182:183] op_sel_hi:[1,1,0]
	v_mov_b32_e32 v194, v159
	v_mul_f32_e32 v178, v158, v170
	s_waitcnt vmcnt(5)
	v_pk_mul_f32 v[242:243], v[148:149], v[190:191]
	v_pk_fma_f32 v[174:175], v[158:159], v[164:165], v[174:175] op_sel_hi:[0,1,1]
	v_mov_b32_e32 v177, v184
	v_mov_b32_e32 v179, v183
	v_mul_f32_e32 v180, v159, v171
	v_pk_mul_f32 v[186:187], v[152:153], v[190:191]
	v_mul_f32_e32 v188, v153, v169
	v_mul_f32_e32 v216, v152, v160
	v_mov_b32_e32 v181, v185
	v_pk_fma_f32 v[242:243], v[148:149], v[172:173], v[242:243] op_sel:[0,0,1] op_sel_hi:[1,1,0]
	v_pk_fma_f32 v[174:175], v[194:195], v[166:167], v[174:175] op_sel_hi:[0,1,1]
	v_pk_add_f32 v[176:177], v[176:177], v[178:179]
	v_pk_mul_f32 v[240:241], v[154:155], v[162:163]
	v_mov_b32_e32 v214, v151
	v_pk_fma_f32 v[186:187], v[152:153], v[172:173], v[186:187] op_sel:[0,0,1] op_sel_hi:[1,1,0]
	v_pk_fma_f32 v[188:189], v[152:153], v[168:169], v[188:189] op_sel_hi:[1,1,0]
	v_pk_fma_f32 v[244:245], v[152:153], v[160:161], v[216:217] op_sel_hi:[1,1,0]
	v_pk_fma_f32 v[184:185], v[150:151], v[164:165], v[242:243] op_sel_hi:[0,1,1]
	v_pk_add_f32 v[120:121], v[120:121], v[174:175]
	v_pk_add_f32 v[174:175], v[180:181], v[176:177]
	v_mov_b32_e32 v212, v155
	v_mul_f32_e32 v192, v154, v170
	v_pk_fma_f32 v[182:183], v[154:155], v[164:165], v[186:187] op_sel_hi:[0,1,1]
	v_mov_b32_e32 v189, v240
	v_mov_b32_e32 v193, v245
	v_pk_add_f32 v[122:123], v[122:123], v[174:175]
	v_pk_fma_f32 v[174:175], v[214:215], v[166:167], v[184:185] op_sel_hi:[0,1,1]
	v_mul_f32_e32 v238, v155, v171
	v_mov_b32_e32 v239, v241
	v_pk_fma_f32 v[178:179], v[212:213], v[166:167], v[182:183] op_sel_hi:[0,1,1]
	v_pk_add_f32 v[182:183], v[188:189], v[192:193]
	v_pk_add_f32 v[88:89], v[174:175], v[88:89]
	v_mul_f32_e32 v174, v149, v169
	v_mul_f32_e32 v180, v148, v160
	v_pk_add_f32 v[176:177], v[238:239], v[182:183]
	v_pk_fma_f32 v[174:175], v[148:149], v[168:169], v[174:175] op_sel_hi:[1,1,0]
	v_pk_fma_f32 v[180:181], v[148:149], v[160:161], v[180:181] op_sel_hi:[1,1,0]
	v_pk_mul_f32 v[182:183], v[150:151], v[162:163]
	v_pk_add_f32 v[106:107], v[106:107], v[176:177]
	v_mul_f32_e32 v176, v150, v170
	v_mov_b32_e32 v175, v182
	v_mov_b32_e32 v177, v181
	v_pk_add_f32 v[104:105], v[178:179], v[104:105]
	v_mul_f32_e32 v178, v151, v171
	v_pk_add_f32 v[174:175], v[174:175], v[176:177]
	v_mov_b32_e32 v179, v183
	v_pk_add_f32 v[174:175], v[178:179], v[174:175]
	s_waitcnt vmcnt(4)
	v_mov_b32_e32 v216, v147
	v_pk_add_f32 v[90:91], v[174:175], v[90:91]
	v_pk_mul_f32 v[174:175], v[144:145], v[190:191]
	v_mul_f32_e32 v180, v144, v160
	v_pk_fma_f32 v[174:175], v[144:145], v[172:173], v[174:175] op_sel:[0,0,1] op_sel_hi:[1,1,0]
	v_pk_fma_f32 v[180:181], v[144:145], v[160:161], v[180:181] op_sel_hi:[1,1,0]
	v_pk_fma_f32 v[174:175], v[146:147], v[164:165], v[174:175] op_sel_hi:[0,1,1]
	v_pk_fma_f32 v[174:175], v[216:217], v[166:167], v[174:175] op_sel_hi:[0,1,1]
	v_pk_add_f32 v[72:73], v[174:175], v[72:73]
	v_mul_f32_e32 v174, v145, v169
	v_pk_fma_f32 v[174:175], v[144:145], v[168:169], v[174:175] op_sel_hi:[1,1,0]
	v_pk_mul_f32 v[182:183], v[146:147], v[162:163]
	v_mul_f32_e32 v176, v146, v170
	v_mov_b32_e32 v175, v182
	v_mov_b32_e32 v177, v181
	v_mul_f32_e32 v178, v147, v171
	v_pk_add_f32 v[174:175], v[174:175], v[176:177]
	v_mov_b32_e32 v179, v183
	v_pk_add_f32 v[186:187], v[178:179], v[174:175]
	v_add_co_u32_e32 v182, vcc, s31, v218
	v_lshl_add_u64 v[188:189], v[218:219], 0, s[12:13]
	s_nop 0
	v_addc_co_u32_e32 v183, vcc, 0, v219, vcc
	v_pk_add_f32 v[74:75], v[186:187], v[74:75]
	s_waitcnt vmcnt(3)
	v_pk_mul_f32 v[186:187], v[140:141], v[190:191]
	global_load_dwordx4 v[174:177], v[188:189], off offset:32
	global_load_dwordx4 v[178:181], v[188:189], off offset:16
	s_nop 0
	global_load_dwordx4 v[182:185], v[182:183], off
	v_pk_fma_f32 v[186:187], v[140:141], v[172:173], v[186:187] op_sel:[0,0,1] op_sel_hi:[1,1,0]
	v_mov_b32_e32 v226, v143
	v_pk_fma_f32 v[186:187], v[142:143], v[164:165], v[186:187] op_sel_hi:[0,1,1]
	v_pk_fma_f32 v[186:187], v[226:227], v[166:167], v[186:187] op_sel_hi:[0,1,1]
	v_pk_add_f32 v[56:57], v[186:187], v[56:57]
	v_mul_f32_e32 v186, v141, v169
	v_pk_fma_f32 v[192:193], v[140:141], v[168:169], v[186:187] op_sel_hi:[1,1,0]
	v_mul_f32_e32 v186, v140, v160
	v_pk_fma_f32 v[242:243], v[140:141], v[160:161], v[186:187] op_sel_hi:[1,1,0]
	global_load_dwordx4 v[186:189], v[188:189], off offset:48
	v_pk_mul_f32 v[244:245], v[142:143], v[162:163]
	v_mul_f32_e32 v238, v142, v170
	v_mov_b32_e32 v193, v244
	v_mov_b32_e32 v239, v243
	v_mul_f32_e32 v240, v143, v171
	v_pk_add_f32 v[192:193], v[192:193], v[238:239]
	v_mov_b32_e32 v241, v245
	v_pk_add_f32 v[192:193], v[240:241], v[192:193]
	s_waitcnt vmcnt(6)
	v_mov_b32_e32 v224, v139
	v_pk_add_f32 v[58:59], v[192:193], v[58:59]
	v_pk_mul_f32 v[192:193], v[136:137], v[190:191]
	v_mul_f32_e32 v220, v136, v160
	v_pk_fma_f32 v[192:193], v[136:137], v[172:173], v[192:193] op_sel:[0,0,1] op_sel_hi:[1,1,0]
	v_pk_fma_f32 v[242:243], v[136:137], v[160:161], v[220:221] op_sel_hi:[1,1,0]
	v_pk_fma_f32 v[192:193], v[138:139], v[164:165], v[192:193] op_sel_hi:[0,1,1]
	v_pk_fma_f32 v[192:193], v[224:225], v[166:167], v[192:193] op_sel_hi:[0,1,1]
	v_pk_add_f32 v[40:41], v[192:193], v[40:41]
	v_mul_f32_e32 v192, v137, v169
	v_pk_fma_f32 v[192:193], v[136:137], v[168:169], v[192:193] op_sel_hi:[1,1,0]
	v_pk_mul_f32 v[244:245], v[138:139], v[162:163]
	v_mul_f32_e32 v238, v138, v170
	v_mov_b32_e32 v193, v244
	v_mov_b32_e32 v239, v243
	v_mul_f32_e32 v240, v139, v171
	v_pk_add_f32 v[192:193], v[192:193], v[238:239]
	v_mov_b32_e32 v241, v245
	v_pk_add_f32 v[192:193], v[240:241], v[192:193]
	s_waitcnt vmcnt(5)
	v_mul_f32_e32 v220, v132, v160
	v_pk_add_f32 v[42:43], v[192:193], v[42:43]
	v_pk_mul_f32 v[192:193], v[132:133], v[190:191]
	s_waitcnt vmcnt(4)
	v_pk_mul_f32 v[190:191], v[128:129], v[190:191]
	v_pk_fma_f32 v[192:193], v[132:133], v[172:173], v[192:193] op_sel:[0,0,1] op_sel_hi:[1,1,0]
	v_pk_fma_f32 v[172:173], v[128:129], v[172:173], v[190:191] op_sel:[0,0,1] op_sel_hi:[1,1,0]
	v_pk_fma_f32 v[192:193], v[134:135], v[164:165], v[192:193] op_sel_hi:[0,1,1]
	v_pk_fma_f32 v[242:243], v[132:133], v[160:161], v[220:221] op_sel_hi:[1,1,0]
	v_pk_fma_f32 v[164:165], v[130:131], v[164:165], v[172:173] op_sel_hi:[0,1,1]
	v_mov_b32_e32 v220, v131
	v_mov_b32_e32 v222, v135
	v_pk_fma_f32 v[164:165], v[220:221], v[166:167], v[164:165] op_sel_hi:[0,1,1]
	v_pk_fma_f32 v[192:193], v[222:223], v[166:167], v[192:193] op_sel_hi:[0,1,1]
	v_mul_f32_e32 v238, v134, v170
	v_pk_add_f32 v[8:9], v[164:165], v[8:9]
	v_mul_f32_e32 v164, v129, v169
	v_mul_f32_e32 v166, v130, v170
	v_mul_f32_e32 v170, v128, v160
	v_pk_mul_f32 v[244:245], v[134:135], v[162:163]
	v_pk_fma_f32 v[164:165], v[128:129], v[168:169], v[164:165] op_sel_hi:[1,1,0]
	v_pk_fma_f32 v[160:161], v[128:129], v[160:161], v[170:171] op_sel_hi:[1,1,0]
	v_pk_mul_f32 v[162:163], v[130:131], v[162:163]
	v_pk_add_f32 v[24:25], v[192:193], v[24:25]
	v_mul_f32_e32 v192, v133, v169
	v_mov_b32_e32 v165, v162
	v_mov_b32_e32 v167, v161
	v_pk_fma_f32 v[192:193], v[132:133], v[168:169], v[192:193] op_sel_hi:[1,1,0]
	v_mul_f32_e32 v168, v131, v171
	v_pk_add_f32 v[160:161], v[164:165], v[166:167]
	v_mov_b32_e32 v169, v163
	v_pk_add_f32 v[160:161], v[168:169], v[160:161]
	v_mov_b32_e32 v193, v244
	v_pk_add_f32 v[10:11], v[160:161], v[10:11]
	v_mov_b32_e32 v239, v243
	v_lshl_add_u64 v[242:243], v[218:219], 0, s[14:15]
	v_mul_f32_e32 v240, v135, v171
	v_pk_add_f32 v[192:193], v[192:193], v[238:239]
	v_mov_b32_e32 v241, v245
	v_pk_add_f32 v[192:193], v[240:241], v[192:193]
	s_waitcnt vmcnt(3)
	v_mul_f32_e32 v162, v158, v176
	s_waitcnt vmcnt(2)
	v_mov_b32_e32 v172, v178
	s_waitcnt vmcnt(1)
	v_mov_b32_e32 v173, v183
	v_pk_mul_f32 v[160:161], v[156:157], v[172:173]
	v_mov_b32_e32 v183, v179
	v_pk_fma_f32 v[160:161], v[156:157], v[182:183], v[160:161] op_sel:[0,0,1] op_sel_hi:[1,1,0]
	v_mov_b32_e32 v178, v184
	v_mov_b32_e32 v179, v180
	v_pk_fma_f32 v[160:161], v[158:159], v[178:179], v[160:161] op_sel_hi:[0,1,1]
	v_mov_b32_e32 v180, v185
	v_pk_fma_f32 v[160:161], v[194:195], v[180:181], v[160:161] op_sel_hi:[0,1,1]
	v_pk_add_f32 v[116:117], v[116:117], v[160:161]
	v_mul_f32_e32 v160, v157, v175
	s_waitcnt vmcnt(0)
	v_mul_f32_e32 v166, v156, v186
	v_pk_fma_f32 v[160:161], v[156:157], v[174:175], v[160:161] op_sel_hi:[1,1,0]
	v_pk_fma_f32 v[166:167], v[156:157], v[186:187], v[166:167] op_sel_hi:[1,1,0]
	v_pk_mul_f32 v[168:169], v[158:159], v[188:189]
	v_mov_b32_e32 v163, v167
	v_mov_b32_e32 v161, v168
	v_mul_f32_e32 v164, v159, v177
	v_pk_add_f32 v[160:161], v[160:161], v[162:163]
	v_mov_b32_e32 v165, v169
	v_pk_add_f32 v[160:161], v[164:165], v[160:161]
	v_mul_f32_e32 v166, v152, v186
	v_pk_add_f32 v[118:119], v[118:119], v[160:161]
	v_pk_mul_f32 v[160:161], v[152:153], v[172:173]
	v_pk_fma_f32 v[166:167], v[152:153], v[186:187], v[166:167] op_sel_hi:[1,1,0]
	v_pk_fma_f32 v[160:161], v[152:153], v[182:183], v[160:161] op_sel:[0,0,1] op_sel_hi:[1,1,0]
	v_pk_mul_f32 v[168:169], v[154:155], v[188:189]
	v_pk_fma_f32 v[160:161], v[154:155], v[178:179], v[160:161] op_sel_hi:[0,1,1]
	v_pk_fma_f32 v[160:161], v[212:213], v[180:181], v[160:161] op_sel_hi:[0,1,1]
	v_pk_add_f32 v[100:101], v[160:161], v[100:101]
	v_mul_f32_e32 v160, v153, v175
	v_pk_fma_f32 v[160:161], v[152:153], v[174:175], v[160:161] op_sel_hi:[1,1,0]
	v_mul_f32_e32 v162, v154, v176
	v_mov_b32_e32 v161, v168
	v_mov_b32_e32 v163, v167
	v_mul_f32_e32 v164, v155, v177
	v_pk_add_f32 v[160:161], v[160:161], v[162:163]
	v_mov_b32_e32 v165, v169
	v_pk_add_f32 v[160:161], v[164:165], v[160:161]
	v_mul_f32_e32 v166, v148, v186
	v_pk_add_f32 v[102:103], v[102:103], v[160:161]
	v_pk_mul_f32 v[160:161], v[148:149], v[172:173]
	v_pk_fma_f32 v[166:167], v[148:149], v[186:187], v[166:167] op_sel_hi:[1,1,0]
	v_pk_fma_f32 v[160:161], v[148:149], v[182:183], v[160:161] op_sel:[0,0,1] op_sel_hi:[1,1,0]
	v_pk_mul_f32 v[168:169], v[150:151], v[188:189]
	v_pk_fma_f32 v[160:161], v[150:151], v[178:179], v[160:161] op_sel_hi:[0,1,1]
	v_pk_fma_f32 v[160:161], v[214:215], v[180:181], v[160:161] op_sel_hi:[0,1,1]
	v_pk_add_f32 v[84:85], v[160:161], v[84:85]
	v_mul_f32_e32 v160, v149, v175
	v_pk_fma_f32 v[160:161], v[148:149], v[174:175], v[160:161] op_sel_hi:[1,1,0]
	v_mul_f32_e32 v162, v150, v176
	v_mov_b32_e32 v161, v168
	v_mov_b32_e32 v163, v167
	v_mul_f32_e32 v164, v151, v177
	v_pk_add_f32 v[160:161], v[160:161], v[162:163]
	v_mov_b32_e32 v165, v169
	v_pk_add_f32 v[160:161], v[164:165], v[160:161]
	v_add_co_u32_e32 v168, vcc, s62, v218
	v_pk_add_f32 v[86:87], v[160:161], v[86:87]
	v_pk_mul_f32 v[160:161], v[144:145], v[172:173]
	v_addc_co_u32_e32 v169, vcc, 0, v219, vcc
	v_pk_fma_f32 v[160:161], v[144:145], v[182:183], v[160:161] op_sel:[0,0,1] op_sel_hi:[1,1,0]
	v_pk_mul_f32 v[240:241], v[146:147], v[188:189]
	v_pk_fma_f32 v[160:161], v[146:147], v[178:179], v[160:161] op_sel_hi:[0,1,1]
	v_pk_fma_f32 v[160:161], v[216:217], v[180:181], v[160:161] op_sel_hi:[0,1,1]
	v_pk_add_f32 v[68:69], v[160:161], v[68:69]
	v_mul_f32_e32 v160, v145, v175
	v_pk_fma_f32 v[184:185], v[144:145], v[174:175], v[160:161] op_sel_hi:[1,1,0]
	v_mul_f32_e32 v160, v144, v186
	v_pk_fma_f32 v[238:239], v[144:145], v[186:187], v[160:161] op_sel_hi:[1,1,0]
	global_load_dwordx4 v[160:163], v[242:243], off offset:32
	global_load_dwordx4 v[164:167], v[242:243], off offset:16
	s_nop 0
	global_load_dwordx4 v[168:171], v[168:169], off
	v_mul_f32_e32 v190, v146, v176
	v_mov_b32_e32 v185, v240
	v_mov_b32_e32 v191, v239
	v_pk_add_f32 v[26:27], v[192:193], v[26:27]
	v_mul_f32_e32 v192, v147, v177
	v_pk_add_f32 v[184:185], v[184:185], v[190:191]
	v_mov_b32_e32 v193, v241
	v_pk_add_f32 v[184:185], v[192:193], v[184:185]
	global_load_dwordx4 v[190:193], v[242:243], off offset:48
	v_pk_add_f32 v[70:71], v[184:185], v[70:71]
	v_pk_mul_f32 v[184:185], v[140:141], v[172:173]
	v_mul_f32_e32 v242, v140, v186
	v_pk_fma_f32 v[184:185], v[140:141], v[182:183], v[184:185] op_sel:[0,0,1] op_sel_hi:[1,1,0]
	v_pk_fma_f32 v[242:243], v[140:141], v[186:187], v[242:243] op_sel_hi:[1,1,0]
	v_pk_fma_f32 v[184:185], v[142:143], v[178:179], v[184:185] op_sel_hi:[0,1,1]
	v_pk_fma_f32 v[184:185], v[226:227], v[180:181], v[184:185] op_sel_hi:[0,1,1]
	v_pk_add_f32 v[52:53], v[184:185], v[52:53]
	v_mul_f32_e32 v184, v141, v175
	v_pk_fma_f32 v[184:185], v[140:141], v[174:175], v[184:185] op_sel_hi:[1,1,0]
	v_pk_mul_f32 v[244:245], v[142:143], v[188:189]
	v_mul_f32_e32 v238, v142, v176
	v_mov_b32_e32 v185, v244
	v_mov_b32_e32 v239, v243
	v_mul_f32_e32 v240, v143, v177
	v_pk_add_f32 v[184:185], v[184:185], v[238:239]
	v_mov_b32_e32 v241, v245
	v_pk_add_f32 v[184:185], v[240:241], v[184:185]
	v_mul_f32_e32 v242, v136, v186
	v_pk_add_f32 v[54:55], v[184:185], v[54:55]
	v_pk_mul_f32 v[184:185], v[136:137], v[172:173]
	v_pk_fma_f32 v[242:243], v[136:137], v[186:187], v[242:243] op_sel_hi:[1,1,0]
	v_pk_fma_f32 v[184:185], v[136:137], v[182:183], v[184:185] op_sel:[0,0,1] op_sel_hi:[1,1,0]
	v_pk_mul_f32 v[244:245], v[138:139], v[188:189]
	v_pk_fma_f32 v[184:185], v[138:139], v[178:179], v[184:185] op_sel_hi:[0,1,1]
	v_pk_fma_f32 v[184:185], v[224:225], v[180:181], v[184:185] op_sel_hi:[0,1,1]
	v_pk_add_f32 v[36:37], v[184:185], v[36:37]
	v_mul_f32_e32 v184, v137, v175
	v_pk_fma_f32 v[184:185], v[136:137], v[174:175], v[184:185] op_sel_hi:[1,1,0]
	v_mul_f32_e32 v238, v138, v176
	v_mov_b32_e32 v185, v244
	v_mov_b32_e32 v239, v243
	v_mul_f32_e32 v240, v139, v177
	v_pk_add_f32 v[184:185], v[184:185], v[238:239]
	v_mov_b32_e32 v241, v245
	v_pk_add_f32 v[184:185], v[240:241], v[184:185]
	v_mul_f32_e32 v238, v134, v176
	v_pk_add_f32 v[38:39], v[184:185], v[38:39]
	v_pk_mul_f32 v[184:185], v[132:133], v[172:173]
	v_pk_mul_f32 v[172:173], v[128:129], v[172:173]
	v_pk_fma_f32 v[184:185], v[132:133], v[182:183], v[184:185] op_sel:[0,0,1] op_sel_hi:[1,1,0]
	v_pk_fma_f32 v[172:173], v[128:129], v[182:183], v[172:173] op_sel:[0,0,1] op_sel_hi:[1,1,0]
	v_pk_fma_f32 v[184:185], v[134:135], v[178:179], v[184:185] op_sel_hi:[0,1,1]
	v_pk_fma_f32 v[172:173], v[130:131], v[178:179], v[172:173] op_sel_hi:[0,1,1]
	v_pk_fma_f32 v[172:173], v[220:221], v[180:181], v[172:173] op_sel_hi:[0,1,1]
	v_pk_fma_f32 v[184:185], v[222:223], v[180:181], v[184:185] op_sel_hi:[0,1,1]
	v_pk_add_f32 v[4:5], v[172:173], v[4:5]
	v_mul_f32_e32 v172, v129, v175
	v_mul_f32_e32 v178, v128, v186
	v_pk_add_f32 v[20:21], v[184:185], v[20:21]
	v_mul_f32_e32 v184, v133, v175
	v_pk_fma_f32 v[172:173], v[128:129], v[174:175], v[172:173] op_sel_hi:[1,1,0]
	v_pk_fma_f32 v[178:179], v[128:129], v[186:187], v[178:179] op_sel_hi:[1,1,0]
	v_pk_mul_f32 v[180:181], v[130:131], v[188:189]
	v_pk_fma_f32 v[184:185], v[132:133], v[174:175], v[184:185] op_sel_hi:[1,1,0]
	v_mul_f32_e32 v174, v130, v176
	v_mov_b32_e32 v173, v180
	v_mov_b32_e32 v175, v179
	v_mul_f32_e32 v240, v135, v177
	v_mul_f32_e32 v242, v132, v186
	v_mul_f32_e32 v176, v131, v177
	v_pk_add_f32 v[172:173], v[172:173], v[174:175]
	v_mov_b32_e32 v177, v181
	v_pk_fma_f32 v[242:243], v[132:133], v[186:187], v[242:243] op_sel_hi:[1,1,0]
	v_pk_add_f32 v[172:173], v[176:177], v[172:173]
	v_pk_mul_f32 v[244:245], v[134:135], v[188:189]
	v_pk_add_f32 v[6:7], v[172:173], v[6:7]
	v_mov_b32_e32 v185, v244
	s_waitcnt vmcnt(3)
	v_mul_f32_e32 v174, v159, v163
	s_waitcnt vmcnt(2)
	v_mov_b32_e32 v186, v164
	s_waitcnt vmcnt(1)
	v_mov_b32_e32 v187, v169
	v_pk_mul_f32 v[172:173], v[156:157], v[186:187]
	v_mov_b32_e32 v169, v165
	v_pk_fma_f32 v[172:173], v[156:157], v[168:169], v[172:173] op_sel:[0,0,1] op_sel_hi:[1,1,0]
	v_mov_b32_e32 v164, v170
	v_mov_b32_e32 v165, v166
	v_pk_fma_f32 v[172:173], v[158:159], v[164:165], v[172:173] op_sel_hi:[0,1,1]
	v_mov_b32_e32 v166, v171
	v_pk_fma_f32 v[170:171], v[194:195], v[166:167], v[172:173] op_sel_hi:[0,1,1]
	v_pk_add_f32 v[124:125], v[124:125], v[170:171]
	v_mul_f32_e32 v170, v157, v161
	s_waitcnt vmcnt(0)
	v_mul_f32_e32 v176, v156, v190
	v_pk_fma_f32 v[170:171], v[156:157], v[160:161], v[170:171] op_sel_hi:[1,1,0]
	v_pk_fma_f32 v[176:177], v[156:157], v[190:191], v[176:177] op_sel_hi:[1,1,0]
	v_pk_mul_f32 v[178:179], v[158:159], v[192:193]
	v_mul_f32_e32 v172, v158, v162
	v_mov_b32_e32 v171, v178
	v_mov_b32_e32 v173, v177
	v_pk_add_f32 v[170:171], v[170:171], v[172:173]
	v_mov_b32_e32 v175, v179
	v_pk_add_f32 v[170:171], v[174:175], v[170:171]
	v_mul_f32_e32 v176, v152, v190
	v_pk_add_f32 v[126:127], v[126:127], v[170:171]
	v_pk_mul_f32 v[170:171], v[152:153], v[186:187]
	v_pk_fma_f32 v[176:177], v[152:153], v[190:191], v[176:177] op_sel_hi:[1,1,0]
	v_pk_fma_f32 v[170:171], v[152:153], v[168:169], v[170:171] op_sel:[0,0,1] op_sel_hi:[1,1,0]
	v_pk_mul_f32 v[178:179], v[154:155], v[192:193]
	v_pk_fma_f32 v[170:171], v[154:155], v[164:165], v[170:171] op_sel_hi:[0,1,1]
	v_pk_fma_f32 v[170:171], v[212:213], v[166:167], v[170:171] op_sel_hi:[0,1,1]
	v_pk_add_f32 v[108:109], v[170:171], v[108:109]
	v_mul_f32_e32 v170, v153, v161
	v_pk_fma_f32 v[170:171], v[152:153], v[160:161], v[170:171] op_sel_hi:[1,1,0]
	v_mul_f32_e32 v172, v154, v162
	v_mov_b32_e32 v171, v178
	v_mov_b32_e32 v173, v177
	v_mul_f32_e32 v174, v155, v163
	v_pk_add_f32 v[170:171], v[170:171], v[172:173]
	v_mov_b32_e32 v175, v179
	v_pk_add_f32 v[170:171], v[174:175], v[170:171]
	v_mul_f32_e32 v176, v148, v190
	v_pk_add_f32 v[110:111], v[110:111], v[170:171]
	v_pk_mul_f32 v[170:171], v[148:149], v[186:187]
	v_pk_fma_f32 v[176:177], v[148:149], v[190:191], v[176:177] op_sel_hi:[1,1,0]
	v_pk_fma_f32 v[170:171], v[148:149], v[168:169], v[170:171] op_sel:[0,0,1] op_sel_hi:[1,1,0]
	v_pk_mul_f32 v[178:179], v[150:151], v[192:193]
	v_pk_fma_f32 v[170:171], v[150:151], v[164:165], v[170:171] op_sel_hi:[0,1,1]
	v_pk_fma_f32 v[170:171], v[214:215], v[166:167], v[170:171] op_sel_hi:[0,1,1]
	v_pk_add_f32 v[92:93], v[170:171], v[92:93]
	v_mul_f32_e32 v170, v149, v161
	v_pk_fma_f32 v[170:171], v[148:149], v[160:161], v[170:171] op_sel_hi:[1,1,0]
	v_mul_f32_e32 v172, v150, v162
	v_mov_b32_e32 v171, v178
	v_mov_b32_e32 v173, v177
	v_mul_f32_e32 v174, v151, v163
	v_pk_add_f32 v[170:171], v[170:171], v[172:173]
	v_mov_b32_e32 v175, v179
	v_pk_add_f32 v[170:171], v[174:175], v[170:171]
	v_mov_b32_e32 v239, v243
	v_pk_add_f32 v[94:95], v[170:171], v[94:95]
	v_pk_mul_f32 v[170:171], v[144:145], v[186:187]
	v_pk_add_f32 v[184:185], v[184:185], v[238:239]
	v_pk_fma_f32 v[170:171], v[144:145], v[168:169], v[170:171] op_sel:[0,0,1] op_sel_hi:[1,1,0]
	v_mov_b32_e32 v241, v245
	v_pk_fma_f32 v[170:171], v[146:147], v[164:165], v[170:171] op_sel_hi:[0,1,1]
	v_pk_fma_f32 v[170:171], v[216:217], v[166:167], v[170:171] op_sel_hi:[0,1,1]
	v_pk_add_f32 v[76:77], v[170:171], v[76:77]
	v_mul_f32_e32 v170, v145, v161
	v_pk_fma_f32 v[182:183], v[144:145], v[160:161], v[170:171] op_sel_hi:[1,1,0]
	v_mul_f32_e32 v170, v144, v190
	v_pk_add_f32 v[184:185], v[240:241], v[184:185]
	v_pk_fma_f32 v[238:239], v[144:145], v[190:191], v[170:171] op_sel_hi:[1,1,0]
	v_pk_mul_f32 v[240:241], v[146:147], v[192:193]
	v_pk_add_f32 v[22:23], v[184:185], v[22:23]
	v_mul_f32_e32 v184, v146, v162
	v_mov_b32_e32 v183, v240
	v_mov_b32_e32 v185, v239
	v_mul_f32_e32 v188, v147, v163
	v_add_co_u32_e32 v178, vcc, s71, v218
	v_pk_add_f32 v[182:183], v[182:183], v[184:185]
	v_mov_b32_e32 v189, v241
	v_lshl_add_u64 v[242:243], v[218:219], 0, s[16:17]
	v_addc_co_u32_e32 v179, vcc, 0, v219, vcc
	v_pk_add_f32 v[182:183], v[188:189], v[182:183]
	global_load_dwordx4 v[170:173], v[242:243], off offset:32
	global_load_dwordx4 v[174:177], v[242:243], off offset:16
	s_nop 0
	global_load_dwordx4 v[178:181], v[178:179], off
	v_pk_add_f32 v[78:79], v[182:183], v[78:79]
	v_pk_mul_f32 v[182:183], v[140:141], v[186:187]
	v_mul_f32_e32 v240, v140, v190
	v_pk_fma_f32 v[182:183], v[140:141], v[168:169], v[182:183] op_sel:[0,0,1] op_sel_hi:[1,1,0]
	v_pk_fma_f32 v[240:241], v[140:141], v[190:191], v[240:241] op_sel_hi:[1,1,0]
	v_pk_fma_f32 v[182:183], v[142:143], v[164:165], v[182:183] op_sel_hi:[0,1,1]
	v_pk_fma_f32 v[182:183], v[226:227], v[166:167], v[182:183] op_sel_hi:[0,1,1]
	v_pk_add_f32 v[60:61], v[182:183], v[60:61]
	v_mul_f32_e32 v182, v141, v161
	v_pk_fma_f32 v[188:189], v[140:141], v[160:161], v[182:183] op_sel_hi:[1,1,0]
	global_load_dwordx4 v[182:185], v[242:243], off offset:48
	v_pk_mul_f32 v[242:243], v[142:143], v[192:193]
	v_mul_f32_e32 v218, v142, v162
	v_mov_b32_e32 v189, v242
	v_mov_b32_e32 v219, v241
	v_mul_f32_e32 v238, v143, v163
	v_pk_add_f32 v[188:189], v[188:189], v[218:219]
	v_mov_b32_e32 v239, v243
	v_pk_add_f32 v[188:189], v[238:239], v[188:189]
	v_mul_f32_e32 v240, v136, v190
	v_pk_add_f32 v[62:63], v[188:189], v[62:63]
	v_pk_mul_f32 v[188:189], v[136:137], v[186:187]
	v_pk_fma_f32 v[240:241], v[136:137], v[190:191], v[240:241] op_sel_hi:[1,1,0]
	v_pk_fma_f32 v[188:189], v[136:137], v[168:169], v[188:189] op_sel:[0,0,1] op_sel_hi:[1,1,0]
	v_pk_mul_f32 v[242:243], v[138:139], v[192:193]
	v_pk_fma_f32 v[188:189], v[138:139], v[164:165], v[188:189] op_sel_hi:[0,1,1]
	v_pk_fma_f32 v[188:189], v[224:225], v[166:167], v[188:189] op_sel_hi:[0,1,1]
	v_pk_add_f32 v[44:45], v[188:189], v[44:45]
	v_mul_f32_e32 v188, v137, v161
	v_pk_fma_f32 v[188:189], v[136:137], v[160:161], v[188:189] op_sel_hi:[1,1,0]
	v_mul_f32_e32 v218, v138, v162
	v_mov_b32_e32 v189, v242
	v_mov_b32_e32 v219, v241
	v_mul_f32_e32 v238, v139, v163
	v_pk_add_f32 v[188:189], v[188:189], v[218:219]
	v_mov_b32_e32 v239, v243
	v_pk_add_f32 v[188:189], v[238:239], v[188:189]
	v_mul_f32_e32 v218, v134, v162
	v_pk_add_f32 v[46:47], v[188:189], v[46:47]
	v_pk_mul_f32 v[188:189], v[132:133], v[186:187]
	v_pk_mul_f32 v[186:187], v[128:129], v[186:187]
	v_pk_fma_f32 v[188:189], v[132:133], v[168:169], v[188:189] op_sel:[0,0,1] op_sel_hi:[1,1,0]
	v_pk_fma_f32 v[168:169], v[128:129], v[168:169], v[186:187] op_sel:[0,0,1] op_sel_hi:[1,1,0]
	v_pk_fma_f32 v[188:189], v[134:135], v[164:165], v[188:189] op_sel_hi:[0,1,1]
	v_pk_fma_f32 v[164:165], v[130:131], v[164:165], v[168:169] op_sel_hi:[0,1,1]
	v_pk_fma_f32 v[188:189], v[222:223], v[166:167], v[188:189] op_sel_hi:[0,1,1]
	v_pk_fma_f32 v[164:165], v[220:221], v[166:167], v[164:165] op_sel_hi:[0,1,1]
	v_pk_add_f32 v[28:29], v[188:189], v[28:29]
	v_mul_f32_e32 v188, v133, v161
	v_pk_add_f32 v[12:13], v[164:165], v[12:13]
	v_mul_f32_e32 v164, v129, v161
	v_mul_f32_e32 v166, v128, v190
	v_pk_fma_f32 v[188:189], v[132:133], v[160:161], v[188:189] op_sel_hi:[1,1,0]
	v_pk_fma_f32 v[160:161], v[128:129], v[160:161], v[164:165] op_sel_hi:[1,1,0]
	v_pk_fma_f32 v[166:167], v[128:129], v[190:191], v[166:167] op_sel_hi:[1,1,0]
	v_pk_mul_f32 v[168:169], v[130:131], v[192:193]
	v_mul_f32_e32 v238, v135, v163
	v_mul_f32_e32 v162, v130, v162
	v_mul_f32_e32 v164, v131, v163
	v_mov_b32_e32 v161, v168
	v_mov_b32_e32 v163, v167
	v_pk_add_f32 v[160:161], v[160:161], v[162:163]
	v_mov_b32_e32 v165, v169
	v_pk_add_f32 v[160:161], v[164:165], v[160:161]
	v_mul_f32_e32 v240, v132, v190
	v_pk_add_f32 v[14:15], v[160:161], v[14:15]
	v_pk_fma_f32 v[240:241], v[132:133], v[190:191], v[240:241] op_sel_hi:[1,1,0]
	v_pk_mul_f32 v[242:243], v[134:135], v[192:193]
	v_mov_b32_e32 v219, v241
	v_mov_b32_e32 v189, v242
	v_pk_add_f32 v[188:189], v[188:189], v[218:219]
	v_mov_b32_e32 v239, v243
	v_pk_add_f32 v[188:189], v[238:239], v[188:189]
	s_waitcnt vmcnt(3)
	v_mul_f32_e32 v166, v158, v172
	s_waitcnt vmcnt(2)
	v_mov_b32_e32 v160, v174
	s_waitcnt vmcnt(1)
	v_mov_b32_e32 v161, v179
	v_pk_mul_f32 v[162:163], v[156:157], v[160:161]
	v_mov_b32_e32 v179, v175
	v_pk_fma_f32 v[162:163], v[156:157], v[178:179], v[162:163] op_sel:[0,0,1] op_sel_hi:[1,1,0]
	v_mov_b32_e32 v164, v180
	v_mov_b32_e32 v165, v176
	v_pk_fma_f32 v[162:163], v[158:159], v[164:165], v[162:163] op_sel_hi:[0,1,1]
	v_mov_b32_e32 v176, v181
	v_pk_fma_f32 v[162:163], v[194:195], v[176:177], v[162:163] op_sel_hi:[0,1,1]
	v_pk_add_f32 v[112:113], v[112:113], v[162:163]
	v_mul_f32_e32 v162, v157, v171
	s_waitcnt vmcnt(0)
	v_mul_f32_e32 v174, v156, v182
	v_pk_fma_f32 v[162:163], v[156:157], v[170:171], v[162:163] op_sel_hi:[1,1,0]
	v_mul_f32_e32 v168, v159, v173
	v_pk_fma_f32 v[156:157], v[156:157], v[182:183], v[174:175] op_sel_hi:[1,1,0]
	v_pk_mul_f32 v[158:159], v[158:159], v[184:185]
	v_mov_b32_e32 v167, v157
	v_mov_b32_e32 v163, v158
	v_pk_add_f32 v[156:157], v[162:163], v[166:167]
	v_mov_b32_e32 v169, v159
	v_pk_add_f32 v[156:157], v[168:169], v[156:157]
	v_mul_f32_e32 v166, v152, v182
	v_pk_add_f32 v[114:115], v[114:115], v[156:157]
	v_pk_mul_f32 v[156:157], v[152:153], v[160:161]
	v_mul_f32_e32 v158, v154, v172
	v_pk_fma_f32 v[156:157], v[152:153], v[178:179], v[156:157] op_sel:[0,0,1] op_sel_hi:[1,1,0]
	v_mul_f32_e32 v162, v155, v173
	v_pk_fma_f32 v[156:157], v[154:155], v[164:165], v[156:157] op_sel_hi:[0,1,1]
	v_pk_fma_f32 v[156:157], v[212:213], v[176:177], v[156:157] op_sel_hi:[0,1,1]
	v_pk_add_f32 v[96:97], v[156:157], v[96:97]
	v_mul_f32_e32 v156, v153, v171
	v_pk_fma_f32 v[156:157], v[152:153], v[170:171], v[156:157] op_sel_hi:[1,1,0]
	v_pk_fma_f32 v[152:153], v[152:153], v[182:183], v[166:167] op_sel_hi:[1,1,0]
	v_pk_mul_f32 v[154:155], v[154:155], v[184:185]
	v_mov_b32_e32 v159, v153
	v_mov_b32_e32 v157, v154
	v_pk_add_f32 v[152:153], v[156:157], v[158:159]
	v_mov_b32_e32 v163, v155
	v_pk_add_f32 v[152:153], v[162:163], v[152:153]
	v_mul_f32_e32 v158, v148, v182
	v_pk_add_f32 v[98:99], v[98:99], v[152:153]
	v_pk_mul_f32 v[152:153], v[148:149], v[160:161]
	v_mul_f32_e32 v154, v150, v172
	v_pk_fma_f32 v[152:153], v[148:149], v[178:179], v[152:153] op_sel:[0,0,1] op_sel_hi:[1,1,0]
	v_mul_f32_e32 v156, v151, v173
	v_pk_fma_f32 v[152:153], v[150:151], v[164:165], v[152:153] op_sel_hi:[0,1,1]
	v_pk_fma_f32 v[152:153], v[214:215], v[176:177], v[152:153] op_sel_hi:[0,1,1]
	v_pk_add_f32 v[80:81], v[152:153], v[80:81]
	v_mul_f32_e32 v152, v149, v171
	v_pk_fma_f32 v[152:153], v[148:149], v[170:171], v[152:153] op_sel_hi:[1,1,0]
	v_pk_fma_f32 v[148:149], v[148:149], v[182:183], v[158:159] op_sel_hi:[1,1,0]
	v_pk_mul_f32 v[150:151], v[150:151], v[184:185]
	v_mov_b32_e32 v155, v149
	v_mov_b32_e32 v153, v150
	v_pk_add_f32 v[148:149], v[152:153], v[154:155]
	v_mov_b32_e32 v157, v151
	v_pk_add_f32 v[148:149], v[156:157], v[148:149]
	v_mul_f32_e32 v154, v144, v182
	v_pk_add_f32 v[82:83], v[148:149], v[82:83]
	v_pk_mul_f32 v[148:149], v[144:145], v[160:161]
	v_mul_f32_e32 v150, v146, v172
	v_pk_fma_f32 v[148:149], v[144:145], v[178:179], v[148:149] op_sel:[0,0,1] op_sel_hi:[1,1,0]
	v_mul_f32_e32 v152, v147, v173
	v_pk_fma_f32 v[148:149], v[146:147], v[164:165], v[148:149] op_sel_hi:[0,1,1]
	v_pk_fma_f32 v[148:149], v[216:217], v[176:177], v[148:149] op_sel_hi:[0,1,1]
	v_pk_add_f32 v[64:65], v[148:149], v[64:65]
	v_mul_f32_e32 v148, v145, v171
	v_pk_fma_f32 v[148:149], v[144:145], v[170:171], v[148:149] op_sel_hi:[1,1,0]
	v_pk_fma_f32 v[144:145], v[144:145], v[182:183], v[154:155] op_sel_hi:[1,1,0]
	v_pk_mul_f32 v[146:147], v[146:147], v[184:185]
	v_mov_b32_e32 v151, v145
	v_mov_b32_e32 v149, v146
	v_pk_add_f32 v[144:145], v[148:149], v[150:151]
	v_mov_b32_e32 v153, v147
	v_pk_add_f32 v[144:145], v[152:153], v[144:145]
	v_mul_f32_e32 v150, v140, v182
	v_pk_add_f32 v[66:67], v[144:145], v[66:67]
	v_pk_mul_f32 v[144:145], v[140:141], v[160:161]
	v_mul_f32_e32 v146, v142, v172
	v_pk_fma_f32 v[144:145], v[140:141], v[178:179], v[144:145] op_sel:[0,0,1] op_sel_hi:[1,1,0]
	v_mul_f32_e32 v148, v143, v173
	v_pk_fma_f32 v[144:145], v[142:143], v[164:165], v[144:145] op_sel_hi:[0,1,1]
	v_pk_fma_f32 v[144:145], v[226:227], v[176:177], v[144:145] op_sel_hi:[0,1,1]
	v_pk_add_f32 v[48:49], v[144:145], v[48:49]
	v_mul_f32_e32 v144, v141, v171
	v_pk_fma_f32 v[144:145], v[140:141], v[170:171], v[144:145] op_sel_hi:[1,1,0]
	v_pk_fma_f32 v[140:141], v[140:141], v[182:183], v[150:151] op_sel_hi:[1,1,0]
	v_pk_mul_f32 v[142:143], v[142:143], v[184:185]
	v_mov_b32_e32 v147, v141
	v_mov_b32_e32 v145, v142
	v_pk_add_f32 v[140:141], v[144:145], v[146:147]
	v_mov_b32_e32 v149, v143
	v_pk_add_f32 v[140:141], v[148:149], v[140:141]
	v_mul_f32_e32 v146, v136, v182
	v_pk_add_f32 v[50:51], v[140:141], v[50:51]
	v_pk_mul_f32 v[140:141], v[136:137], v[160:161]
	v_mul_f32_e32 v142, v138, v172
	v_pk_fma_f32 v[140:141], v[136:137], v[178:179], v[140:141] op_sel:[0,0,1] op_sel_hi:[1,1,0]
	v_mul_f32_e32 v144, v139, v173
	v_pk_fma_f32 v[140:141], v[138:139], v[164:165], v[140:141] op_sel_hi:[0,1,1]
	v_pk_fma_f32 v[140:141], v[224:225], v[176:177], v[140:141] op_sel_hi:[0,1,1]
	v_pk_add_f32 v[32:33], v[140:141], v[32:33]
	v_mul_f32_e32 v140, v137, v171
	v_pk_fma_f32 v[140:141], v[136:137], v[170:171], v[140:141] op_sel_hi:[1,1,0]
	v_pk_fma_f32 v[136:137], v[136:137], v[182:183], v[146:147] op_sel_hi:[1,1,0]
	v_pk_mul_f32 v[138:139], v[138:139], v[184:185]
	v_mov_b32_e32 v143, v137
	v_mov_b32_e32 v141, v138
	v_pk_add_f32 v[136:137], v[140:141], v[142:143]
	v_mov_b32_e32 v145, v139
	v_pk_add_f32 v[136:137], v[144:145], v[136:137]
	v_mul_f32_e32 v142, v132, v182
	v_pk_add_f32 v[34:35], v[136:137], v[34:35]
	v_pk_mul_f32 v[136:137], v[132:133], v[160:161]
	v_mul_f32_e32 v138, v134, v172
	v_pk_fma_f32 v[136:137], v[132:133], v[178:179], v[136:137] op_sel:[0,0,1] op_sel_hi:[1,1,0]
	v_mul_f32_e32 v140, v135, v173
	v_pk_fma_f32 v[136:137], v[134:135], v[164:165], v[136:137] op_sel_hi:[0,1,1]
	v_pk_fma_f32 v[136:137], v[222:223], v[176:177], v[136:137] op_sel_hi:[0,1,1]
	v_pk_add_f32 v[16:17], v[136:137], v[16:17]
	v_mul_f32_e32 v136, v133, v171
	v_pk_fma_f32 v[136:137], v[132:133], v[170:171], v[136:137] op_sel_hi:[1,1,0]
	v_pk_fma_f32 v[132:133], v[132:133], v[182:183], v[142:143] op_sel_hi:[1,1,0]
	v_pk_mul_f32 v[134:135], v[134:135], v[184:185]
	v_mov_b32_e32 v139, v133
	v_mov_b32_e32 v137, v134
	v_pk_add_f32 v[132:133], v[136:137], v[138:139]
	v_mov_b32_e32 v141, v135
	v_pk_add_f32 v[132:133], v[140:141], v[132:133]
	v_mul_f32_e32 v138, v128, v182
	v_pk_add_f32 v[18:19], v[132:133], v[18:19]
	v_pk_mul_f32 v[132:133], v[128:129], v[160:161]
	v_mul_f32_e32 v134, v130, v172
	v_pk_fma_f32 v[132:133], v[128:129], v[178:179], v[132:133] op_sel:[0,0,1] op_sel_hi:[1,1,0]
	v_mul_f32_e32 v136, v131, v173
	v_pk_fma_f32 v[132:133], v[130:131], v[164:165], v[132:133] op_sel_hi:[0,1,1]
	v_pk_fma_f32 v[132:133], v[220:221], v[176:177], v[132:133] op_sel_hi:[0,1,1]
	v_pk_add_f32 v[0:1], v[132:133], v[0:1]
	v_mul_f32_e32 v132, v129, v171
	v_pk_fma_f32 v[132:133], v[128:129], v[170:171], v[132:133] op_sel_hi:[1,1,0]
	v_pk_fma_f32 v[128:129], v[128:129], v[182:183], v[138:139] op_sel_hi:[1,1,0]
	v_pk_mul_f32 v[130:131], v[130:131], v[184:185]
	v_mov_b32_e32 v135, v129
	v_mov_b32_e32 v133, v130
	v_pk_add_f32 v[128:129], v[132:133], v[134:135]
	v_mov_b32_e32 v137, v131
	v_pk_add_f32 v[128:129], v[136:137], v[128:129]
	v_pk_add_f32 v[30:31], v[188:189], v[30:31]
	v_pk_add_f32 v[2:3], v[128:129], v[2:3]

.LBB2_93:
	s_waitcnt vmcnt(0)
.LBB2_95:
	s_barrier
